# v69 with 121 converter CUs in P2 (135 GEMM CUs, still 5+10 rounds)
# speedup vs baseline: 1.0016x; 1.0016x over previous
;     __device__ __forceinline__ bool next(int i, Unit& u) const { const int L = i * G + c; if (L >= 2 * SSMG) return false; u.pm = L; u.pn = L >> 1; return true; }
;     __device__ __forceinline__ bool next(int i, Unit& u) const { const int L = i * G + c; if (L >= 256) return false; const int g = L >> 2; u.pm = 2 * g + ((L >> 1) & 1); u.pn = 2 * g + (L & 1); return true; }
; #define REPS(k) _Pragma("unroll") for (int rep_ = 0; rep_ < 1 + ((PROBE_REP >> (k)) & 1); ++rep_)
;     __host__ __device__ bool next(int i, Unit& u) const {
;         const long L = (long)i * G + c; if (L >= nwg) return false;
;         int wgid = (int)L; { const int q = nwg / NXCD, r = nwg % NXCD, xcd = wgid % NXCD, off = wgid / NXCD; wgid = (xcd < r ? xcd * (q + 1) : r * (q + 1) + (xcd - r) * q) + off; }
;         const int nig = WGM * nN, gid = wgid / nig, fm = gid * WGM, gsz = (nM - fm) < WGM ? (nM - fm) : WGM;
;         u.pm = fm + ((wgid % nig) % gsz); u.pn = (wgid % nig) / gsz; return true;
; __global__ void __launch_bounds__(NTHR, 2) fwd(Args args) {
;     ...
;     if (IN(2)) REPS(2) {
;         const int Gg = (G > 2 * NCONV) ? G - NCONV : G;
;         if (bid < Gg) {
;             { pg8::Gemm g{(const bf16*)(ws + WS_HN), (const bf16*)(ws + WS_WIN), DM, DM, DM}; pg8::StaticOrder S; S.init(T, 2560, Gg, bid);
;               EpiInProjA E{(bf16*)(ws + WS_Q), (bf16*)(ws + WS_K), (bf16*)(ws + WS_IQ), (bf16*)(ws + WS_IK), (float*)(ws + WS_IW)};
;               pg8::gemm_phase<EpiInProjA, pg8::StaticOrder, true, true>(lds, g, S, E); }
.LBB0_388:
	v_readlane_b32 s2, v250, 11
	v_readlane_b32 s3, v250, 12
	s_cmp_lt_i32 s2, 3
	s_cselect_b64 s[2:3], -1, 0
	s_and_b64 s[0:1], s[2:3], s[0:1]
	s_andn2_b64 vcc, exec, s[0:1]
	s_cbranch_vccnz .LBB0_515
	s_add_i32 s0, s88, 0xffffff87
	s_cmpk_gt_i32 s88, 0xf0
	s_cselect_b32 s4, s0, s88
	v_writelane_b32 v250, s2, 58
	s_cmp_ge_i32 s84, s4
	s_nop 0
	v_writelane_b32 v250, s3, 59
	s_cbranch_scc1 .LBB0_490
	s_cmpk_lt_i32 s84, 0x280
	s_cselect_b64 s[0:1], -1, 0
	s_ashr_i32 s5, s84, 31
	s_lshr_b32 s2, s5, 29
	s_add_i32 s2, s84, s2
	s_ashr_i32 s25, s2, 3
	s_and_b32 s2, s2, -8
	s_sub_i32 s46, s84, s2
	s_cmp_lt_i32 s46, 0
	s_cselect_b64 s[6:7], -1, 0
	s_cmpk_gt_i32 s84, 0x27f
	v_readfirstlane_b32 s22, v0
	s_cbranch_scc1 .LBB0_392
	s_movk_i32 s8, 0x51
	s_and_b64 s[2:3], s[6:7], exec
	s_cselect_b32 s2, s8, 0x50
	s_mul_i32 s2, s46, s2
	s_add_i32 s2, s2, s25
	s_mul_hi_i32 s3, s2, 0x66666667
	s_lshr_b32 s8, s3, 31
	s_ashr_i32 s3, s3, 5
	s_add_i32 s3, s3, s8
	s_lshl_b32 s8, s3, 3
	s_mulk_i32 s3, 0x50
	s_sub_i32 s2, s2, s3
	s_bfe_i32 s3, s2, 0x80000
	s_bfe_u32 s3, s3, 0x3000c
	s_add_i32 s3, s2, s3
	s_bfe_i32 s9, s3, 0x80000
	s_and_b32 s3, s3, 0xf8
	s_sub_i32 s2, s2, s3
	s_sext_i32_i16 s9, s9
	s_sext_i32_i8 s2, s2
	s_add_i32 s2, s8, s2
	s_ashr_i32 s36, s9, 3
